# speedup vs baseline: 1.0256x; 1.0103x over previous
_Z9ssim_mainPKfS0_S0_Pf:
	v_readfirstlane_b32 s29, v0
	s_load_dwordx4 s[4:7], s[0:1], 0x0
	s_load_dwordx4 s[8:11], s[0:1], 0x10
	s_mov_b32 s51, 0x44800000
	s_mov_b32 s38, 0
	s_mov_b32 s39, -1
	s_lshr_b32 s12, s29, 6
	s_and_b32 s13, s2, 7
	s_lshl_b32 s13, s13, 5
	s_lshr_b32 s14, s2, 3
	s_add_u32 s13, s13, s14
	s_lshr_b32 s14, s13, 3
	s_and_b32 s15, s13, 7
	s_lshl_b32 s16, s14, 20
	s_lshl_b32 s17, s15, 17
	s_add_u32 s16, s16, s17
	s_lshl_b32 s17, s12, 8
	s_add_u32 s16, s16, s17
	s_lshl_b32 s27, s12, 2
	s_add_u32 s27, s27, 0x10000
	v_and_b32_e32 v8, 63, v0
	v_and_b32_e32 v169, 15, v0
	v_bfe_u32 v164, v0, 4, 2
	v_mov_b32_e32 v6, s27
	v_mov_b32_e32 v168, 0
	ds_write_b32 v6, v168 offset:0
	ds_write_b32 v6, v168 offset:32
	ds_write_b32 v6, v168 offset:64
	ds_write_b32 v6, v168 offset:96
	v_lshrrev_b32_e32 v167, 2, v169
	v_lshlrev_b32_e32 v167, 5, v167
	v_and_b32_e32 v168, 1, v169
	v_lshl_or_b32 v167, v168, 4, v167
	v_bfe_u32 v168, v169, 1, 1
	v_lshl_or_b32 v167, v168, 7, v167
	v_lshl_or_b32 v9, v164, 14, v167
	v_and_b32_e32 v168, 1, v164
	v_lshl_or_b32 v23, v168, 14, v167
	v_lshrrev_b32_e32 v168, 1, v164
	v_lshl_or_b32 v23, v168, 13, v23
	v_add_u32_e32 v237, 0x1000, v9
	v_add_u32_e32 v238, 0x2000, v9
	v_add_u32_e32 v239, 0x3000, v9
	v_add_u32_e32 v240, 0x10000, v9
	v_add_u32_e32 v241, 0x11000, v9
	v_add_u32_e32 v242, 0x12000, v9
	v_add_u32_e32 v243, 0x13000, v9
	s_waitcnt lgkmcnt(0)
	s_add_u32 s18, s4, s16
	s_addc_u32 s19, s5, 0
	s_add_u32 s20, s6, s16
	s_addc_u32 s21, s7, 0
	global_load_dwordx4 v[36:39], v9, s[18:19] offset:0 sc1 nt
	global_load_dwordx4 v[40:43], v9, s[18:19] offset:2048 sc1 nt
	global_load_dwordx4 v[68:71], v9, s[20:21] offset:0 sc1 nt
	global_load_dwordx4 v[72:75], v9, s[20:21] offset:2048 sc1 nt
	global_load_dwordx4 v[44:47], v237, s[18:19] offset:0 sc1 nt
	global_load_dwordx4 v[48:51], v237, s[18:19] offset:2048 sc1 nt
	global_load_dwordx4 v[76:79], v237, s[20:21] offset:0 sc1 nt
	global_load_dwordx4 v[80:83], v237, s[20:21] offset:2048 sc1 nt
	global_load_dwordx4 v[52:55], v238, s[18:19] offset:0 sc1 nt
	global_load_dwordx4 v[56:59], v238, s[18:19] offset:2048 sc1 nt
	global_load_dwordx4 v[84:87], v238, s[20:21] offset:0 sc1 nt
	global_load_dwordx4 v[88:91], v238, s[20:21] offset:2048 sc1 nt
	global_load_dwordx4 v[60:63], v239, s[18:19] offset:0 sc1 nt
	global_load_dwordx4 v[64:67], v239, s[18:19] offset:2048 sc1 nt
	global_load_dwordx4 v[92:95], v239, s[20:21] offset:0 sc1 nt
	global_load_dwordx4 v[96:99], v239, s[20:21] offset:2048 sc1 nt
	v_lshlrev_b32_e32 v167, 3, v164
	v_xor_b32_e32 v168, 16, v167
	v_sub_u32_e32 v165, v167, v169
	v_sub_u32_e32 v166, v168, v169
	v_add_u32_e32 v172, 0, v165
	v_med3_i32 v172, v172, 0, 10
	v_lshlrev_b32_e32 v172, 2, v172
	v_add_u32_e32 v173, 1, v165
	v_med3_i32 v173, v173, 0, 10
	v_lshlrev_b32_e32 v173, 2, v173
	v_add_u32_e32 v174, 2, v165
	v_med3_i32 v174, v174, 0, 10
	v_lshlrev_b32_e32 v174, 2, v174
	v_add_u32_e32 v175, 3, v165
	v_med3_i32 v175, v175, 0, 10
	v_lshlrev_b32_e32 v175, 2, v175
	v_add_u32_e32 v176, 4, v165
	v_med3_i32 v176, v176, 0, 10
	v_lshlrev_b32_e32 v176, 2, v176
	v_add_u32_e32 v177, 5, v165
	v_med3_i32 v177, v177, 0, 10
	v_lshlrev_b32_e32 v177, 2, v177
	v_add_u32_e32 v178, 6, v165
	v_med3_i32 v178, v178, 0, 10
	v_lshlrev_b32_e32 v178, 2, v178
	v_add_u32_e32 v179, 7, v165
	v_med3_i32 v179, v179, 0, 10
	v_lshlrev_b32_e32 v179, 2, v179
	v_add_u32_e32 v180, 0, v166
	v_med3_i32 v180, v180, 0, 10
	v_lshlrev_b32_e32 v180, 2, v180
	v_add_u32_e32 v181, 1, v166
	v_med3_i32 v181, v181, 0, 10
	v_lshlrev_b32_e32 v181, 2, v181
	v_add_u32_e32 v182, 2, v166
	v_med3_i32 v182, v182, 0, 10
	v_lshlrev_b32_e32 v182, 2, v182
	v_add_u32_e32 v183, 3, v166
	v_med3_i32 v183, v183, 0, 10
	v_lshlrev_b32_e32 v183, 2, v183
	v_add_u32_e32 v184, 4, v166
	v_med3_i32 v184, v184, 0, 10
	v_lshlrev_b32_e32 v184, 2, v184
	v_add_u32_e32 v185, 5, v166
	v_med3_i32 v185, v185, 0, 10
	v_lshlrev_b32_e32 v185, 2, v185
	v_add_u32_e32 v186, 6, v166
	v_med3_i32 v186, v186, 0, 10
	v_lshlrev_b32_e32 v186, 2, v186
	v_add_u32_e32 v187, 7, v166
	v_med3_i32 v187, v187, 0, 10
	v_lshlrev_b32_e32 v187, 2, v187
	global_load_dword v188, v172, s[8:9]
	global_load_dword v189, v173, s[8:9]
	global_load_dword v190, v174, s[8:9]
	global_load_dword v191, v175, s[8:9]
	global_load_dword v192, v176, s[8:9]
	global_load_dword v193, v177, s[8:9]
	global_load_dword v194, v178, s[8:9]
	global_load_dword v195, v179, s[8:9]
	global_load_dword v196, v180, s[8:9]
	global_load_dword v197, v181, s[8:9]
	global_load_dword v198, v182, s[8:9]
	global_load_dword v199, v183, s[8:9]
	global_load_dword v200, v184, s[8:9]
	global_load_dword v201, v185, s[8:9]
	global_load_dword v202, v186, s[8:9]
	global_load_dword v203, v187, s[8:9]
	s_load_dwordx8 s[40:47], s[8:9], 0x0
	s_load_dwordx2 s[48:49], s[8:9], 0x20
	s_load_dword s50, s[8:9], 0x28
	global_load_dwordx4 v[100:103], v240, s[18:19] offset:0 sc1 nt
	global_load_dwordx4 v[104:107], v240, s[18:19] offset:2048 sc1 nt
	global_load_dwordx4 v[132:135], v240, s[20:21] offset:0 sc1 nt
	global_load_dwordx4 v[136:139], v240, s[20:21] offset:2048 sc1 nt
	global_load_dwordx4 v[108:111], v241, s[18:19] offset:0 sc1 nt
	global_load_dwordx4 v[112:115], v241, s[18:19] offset:2048 sc1 nt
	global_load_dwordx4 v[140:143], v241, s[20:21] offset:0 sc1 nt
	global_load_dwordx4 v[144:147], v241, s[20:21] offset:2048 sc1 nt
	global_load_dwordx4 v[116:119], v242, s[18:19] offset:0 sc1 nt
	global_load_dwordx4 v[120:123], v242, s[18:19] offset:2048 sc1 nt
	global_load_dwordx4 v[148:151], v242, s[20:21] offset:0 sc1 nt
	global_load_dwordx4 v[152:155], v242, s[20:21] offset:2048 sc1 nt
	global_load_dwordx4 v[124:127], v243, s[18:19] offset:0 sc1 nt
	global_load_dwordx4 v[128:131], v243, s[18:19] offset:2048 sc1 nt
	global_load_dwordx4 v[156:159], v243, s[20:21] offset:0 sc1 nt
	global_load_dwordx4 v[160:163], v243, s[20:21] offset:2048 sc1 nt
	s_cmp_eq_u32 s15, 7
	s_cselect_b32 s22, 0, 0x20000
	s_add_u32 s84, s18, s22
	s_addc_u32 s85, s19, 0
	s_add_u32 s86, s18, s22
	s_addc_u32 s87, s19, 0
	s_add_u32 s86, s86, 0x1000
	s_addc_u32 s87, s87, 0
	s_add_u32 s88, s20, s22
	s_addc_u32 s89, s21, 0
	s_add_u32 s90, s20, s22
	s_addc_u32 s91, s21, 0
	s_add_u32 s90, s90, 0x1000
	s_addc_u32 s91, s91, 0
	s_waitcnt lgkmcnt(0)
	v_mov_b32_e32 v229, 0x44800000
	v_fma_mixlo_f16 v228, s40, v229, 0
	v_cvt_f32_f16_e32 v228, v228
	v_cvt_f64_f32_e32 v[212:213], v228
	v_add_f64 v[212:213], v[212:213], 0
	v_fma_mixlo_f16 v228, s41, v229, 0
	v_cvt_f32_f16_e32 v228, v228
	v_cvt_f64_f32_e32 v[214:215], v228
	v_add_f64 v[212:213], v[212:213], v[214:215]
	v_fma_mixlo_f16 v228, s42, v229, 0
	v_cvt_f32_f16_e32 v228, v228
	v_cvt_f64_f32_e32 v[214:215], v228
	v_add_f64 v[212:213], v[212:213], v[214:215]
	v_fma_mixlo_f16 v228, s43, v229, 0
	v_cvt_f32_f16_e32 v228, v228
	v_cvt_f64_f32_e32 v[214:215], v228
	v_add_f64 v[212:213], v[212:213], v[214:215]
	v_fma_mixlo_f16 v228, s44, v229, 0
	v_cvt_f32_f16_e32 v228, v228
	v_cvt_f64_f32_e32 v[214:215], v228
	v_add_f64 v[212:213], v[212:213], v[214:215]
	v_fma_mixlo_f16 v228, s45, v229, 0
	v_cvt_f32_f16_e32 v228, v228
	v_cvt_f64_f32_e32 v[214:215], v228
	v_add_f64 v[212:213], v[212:213], v[214:215]
	v_fma_mixlo_f16 v228, s46, v229, 0
	v_cvt_f32_f16_e32 v228, v228
	v_cvt_f64_f32_e32 v[214:215], v228
	v_add_f64 v[212:213], v[212:213], v[214:215]
	v_fma_mixlo_f16 v228, s47, v229, 0
	v_cvt_f32_f16_e32 v228, v228
	v_cvt_f64_f32_e32 v[214:215], v228
	v_add_f64 v[212:213], v[212:213], v[214:215]
	v_fma_mixlo_f16 v228, s48, v229, 0
	v_cvt_f32_f16_e32 v228, v228
	v_cvt_f64_f32_e32 v[214:215], v228
	v_add_f64 v[212:213], v[212:213], v[214:215]
	v_fma_mixlo_f16 v228, s49, v229, 0
	v_cvt_f32_f16_e32 v228, v228
	v_cvt_f64_f32_e32 v[214:215], v228
	v_add_f64 v[212:213], v[212:213], v[214:215]
	v_fma_mixlo_f16 v228, s50, v229, 0
	v_cvt_f32_f16_e32 v228, v228
	v_cvt_f64_f32_e32 v[214:215], v228
	v_add_f64 v[212:213], v[212:213], v[214:215]
	v_mul_f64 v[212:213], v[212:213], v[212:213]
	v_mul_f64 v[216:217], v[212:213], 0.5
	v_add_f64 v[218:219], v[216:217], v[216:217]
	s_mov_b32 s36, 0xeb1c432d
	s_mov_b32 s37, 0x3f1a36e2
	v_mul_f64 v[220:221], v[212:213], s[36:37]
	v_mul_f64 v[222:223], v[216:217], v[218:219]
	v_fmac_f64_e32 v[222:223], v[212:213], v[220:221]
	v_add_f64 v[224:225], v[212:213], v[212:213]
	s_mov_b32 s36, 0x487fcb92
	s_mov_b32 s37, 0x3f4d7dbf
	v_mul_f64 v[226:227], v[212:213], s[36:37]
	v_cvt_f32_f64_e32 v0, v[226:227]
	v_mov_b32_e32 v1, v0
	v_mov_b32_e32 v2, v0
	v_mov_b32_e32 v3, v0
	v_cvt_f32_f64_e32 v10, v[218:219]
	v_cvt_f32_f64_e32 v11, v[222:223]
	v_cvt_f32_f64_e32 v12, v[212:213]
	v_cvt_f32_f64_e32 v13, v[224:225]
	v_mul_f64 v[226:227], v[212:213], v[226:227]
	v_cvt_f32_f64_e32 v14, v[226:227]
	v_lshlrev_b32_e32 v167, 2, v164
	s_cmp_eq_u32 s12, 0
	s_cselect_b32 s23, 6, 64
	v_add_u32_e32 v168, 0, v167
	v_cmp_gt_u32_e32 vcc, s23, v168
	s_nop 1
	v_cndmask_b32_e64 v15, 0, 1.0, vcc
	v_add_u32_e32 v168, 1, v167
	v_cmp_gt_u32_e32 vcc, s23, v168
	s_nop 1
	v_cndmask_b32_e64 v16, 0, 1.0, vcc
	v_add_u32_e32 v168, 2, v167
	v_cmp_gt_u32_e32 vcc, s23, v168
	s_nop 1
	v_cndmask_b32_e64 v17, 0, 1.0, vcc
	v_add_u32_e32 v168, 3, v167
	v_cmp_gt_u32_e32 vcc, s23, v168
	s_nop 1
	v_cndmask_b32_e64 v18, 0, 1.0, vcc
	v_and_b32_e32 v167, 31, v8
	v_lshlrev_b32_e32 v167, 4, v167
	s_lshl_b32 s24, s12, 11
	s_add_i32 s25, s12, 7
	s_and_b32 s25, s25, 7
	s_lshl_b32 s26, s25, 11
	v_or_b32_e32 v4, s24, v167
	v_or_b32_e32 v5, s26, v167
	s_lshl_b32 s28, s25, 2
	s_add_u32 s28, s28, 0x10000
	v_mov_b32_e32 v7, s28
	v_mov_b32_e32 v19, 0
	v_mov_b32_e32 v20, 0
	v_mov_b32_e32 v21, 0
	v_mov_b32_e32 v22, 0
	s_waitcnt vmcnt(16)
	v_cmp_lt_u32_e64 s[32:33], 31, v8
	v_cmp_gt_u32_e64 s[34:35], 32, v8
	v_fma_mixlo_f16 v204, v188, s51, 0
	v_add_u32_e32 v167, 0, v165
	v_cmp_gt_u32_e32 vcc, 11, v167
	s_nop 1
	v_cndmask_b32_e32 v204, 0, v204, vcc
	v_fma_mixlo_f16 v205, v189, s51, 0
	v_add_u32_e32 v167, 1, v165
	v_cmp_gt_u32_e32 vcc, 11, v167
	s_nop 1
	v_cndmask_b32_e32 v205, 0, v205, vcc
	v_fma_mixlo_f16 v206, v190, s51, 0
	v_add_u32_e32 v167, 2, v165
	v_cmp_gt_u32_e32 vcc, 11, v167
	s_nop 1
	v_cndmask_b32_e32 v206, 0, v206, vcc
	v_fma_mixlo_f16 v207, v191, s51, 0
	v_add_u32_e32 v167, 3, v165
	v_cmp_gt_u32_e32 vcc, 11, v167
	s_nop 1
	v_cndmask_b32_e32 v207, 0, v207, vcc
	v_fma_mixlo_f16 v208, v192, s51, 0
	v_add_u32_e32 v167, 4, v165
	v_cmp_gt_u32_e32 vcc, 11, v167
	s_nop 1
	v_cndmask_b32_e32 v208, 0, v208, vcc
	v_fma_mixlo_f16 v209, v193, s51, 0
	v_add_u32_e32 v167, 5, v165
	v_cmp_gt_u32_e32 vcc, 11, v167
	s_nop 1
	v_cndmask_b32_e32 v209, 0, v209, vcc
	v_fma_mixlo_f16 v210, v194, s51, 0
	v_add_u32_e32 v167, 6, v165
	v_cmp_gt_u32_e32 vcc, 11, v167
	s_nop 1
	v_cndmask_b32_e32 v210, 0, v210, vcc
	v_fma_mixlo_f16 v211, v195, s51, 0
	v_add_u32_e32 v167, 7, v165
	v_cmp_gt_u32_e32 vcc, 11, v167
	s_nop 1
	v_cndmask_b32_e32 v211, 0, v211, vcc
	v_pack_b32_f16 v24, v204, v205
	v_pack_b32_f16 v25, v206, v207
	v_pack_b32_f16 v26, v208, v209
	v_pack_b32_f16 v27, v210, v211
	v_fma_mixlo_f16 v204, v196, s51, 0
	v_add_u32_e32 v167, 0, v166
	v_cmp_gt_u32_e32 vcc, 11, v167
	s_nop 1
	v_cndmask_b32_e32 v204, 0, v204, vcc
	v_fma_mixlo_f16 v205, v197, s51, 0
	v_add_u32_e32 v167, 1, v166
	v_cmp_gt_u32_e32 vcc, 11, v167
	s_nop 1
	v_cndmask_b32_e32 v205, 0, v205, vcc
	v_fma_mixlo_f16 v206, v198, s51, 0
	v_add_u32_e32 v167, 2, v166
	v_cmp_gt_u32_e32 vcc, 11, v167
	s_nop 1
	v_cndmask_b32_e32 v206, 0, v206, vcc
	v_fma_mixlo_f16 v207, v199, s51, 0
	v_add_u32_e32 v167, 3, v166
	v_cmp_gt_u32_e32 vcc, 11, v167
	s_nop 1
	v_cndmask_b32_e32 v207, 0, v207, vcc
	v_fma_mixlo_f16 v208, v200, s51, 0
	v_add_u32_e32 v167, 4, v166
	v_cmp_gt_u32_e32 vcc, 11, v167
	s_nop 1
	v_cndmask_b32_e32 v208, 0, v208, vcc
	v_fma_mixlo_f16 v209, v201, s51, 0
	v_add_u32_e32 v167, 5, v166
	v_cmp_gt_u32_e32 vcc, 11, v167
	s_nop 1
	v_cndmask_b32_e32 v209, 0, v209, vcc
	v_fma_mixlo_f16 v210, v202, s51, 0
	v_add_u32_e32 v167, 6, v166
	v_cmp_gt_u32_e32 vcc, 11, v167
	s_nop 1
	v_cndmask_b32_e32 v210, 0, v210, vcc
	v_fma_mixlo_f16 v211, v203, s51, 0
	v_add_u32_e32 v167, 7, v166
	v_cmp_gt_u32_e32 vcc, 11, v167
	s_nop 1
	v_cndmask_b32_e32 v211, 0, v211, vcc
	v_pack_b32_f16 v167, v204, v205
	v_cndmask_b32_e64 v28, 0, v167, s[32:33]
	v_cndmask_b32_e64 v32, 0, v167, s[34:35]
	v_pack_b32_f16 v167, v206, v207
	v_cndmask_b32_e64 v29, 0, v167, s[32:33]
	v_cndmask_b32_e64 v33, 0, v167, s[34:35]
	v_pack_b32_f16 v167, v208, v209
	v_cndmask_b32_e64 v30, 0, v167, s[32:33]
	v_cndmask_b32_e64 v34, 0, v167, s[34:35]
	v_pack_b32_f16 v167, v210, v211
	v_cndmask_b32_e64 v31, 0, v167, s[32:33]
	v_cndmask_b32_e64 v35, 0, v167, s[34:35]
	s_waitcnt lgkmcnt(0)
	s_cmp_lt_u32 s12, 4
	s_cbranch_scc1 .Lq_noprio
	s_setprio 1
.Lq_noprio:
	s_waitcnt vmcnt(16)
	v_cvt_pk_f16_f32 v164, v36, v40
	v_cvt_pk_f16_f32 v180, v68, v72
	v_pk_add_f16 v164, v164, -0.5 op_sel_hi:[1,0]
	v_pk_add_f16 v180, v180, -0.5 op_sel_hi:[1,0]
	v_pk_mul_f16 v196, v180, v180
	v_pk_mul_f16 v212, v164, v180
	v_pk_fma_f16 v196, v164, v164, v196
	v_cvt_pk_f16_f32 v168, v37, v41
	v_cvt_pk_f16_f32 v184, v69, v73
	v_pk_add_f16 v168, v168, -0.5 op_sel_hi:[1,0]
	v_pk_add_f16 v184, v184, -0.5 op_sel_hi:[1,0]
	v_pk_mul_f16 v200, v184, v184
	v_pk_mul_f16 v216, v168, v184
	v_pk_fma_f16 v200, v168, v168, v200
	v_cvt_pk_f16_f32 v172, v38, v42
	v_cvt_pk_f16_f32 v188, v70, v74
	v_pk_add_f16 v172, v172, -0.5 op_sel_hi:[1,0]
	v_pk_add_f16 v188, v188, -0.5 op_sel_hi:[1,0]
	v_pk_mul_f16 v204, v188, v188
	v_pk_mul_f16 v220, v172, v188
	v_pk_fma_f16 v204, v172, v172, v204
	v_cvt_pk_f16_f32 v176, v39, v43
	v_cvt_pk_f16_f32 v192, v71, v75
	v_pk_add_f16 v176, v176, -0.5 op_sel_hi:[1,0]
	v_pk_add_f16 v192, v192, -0.5 op_sel_hi:[1,0]
	v_pk_mul_f16 v208, v192, v192
	v_pk_mul_f16 v224, v176, v192
	v_pk_fma_f16 v208, v176, v176, v208
	s_waitcnt vmcnt(16)
	v_cvt_pk_f16_f32 v165, v44, v48
	v_cvt_pk_f16_f32 v181, v76, v80
	v_pk_add_f16 v165, v165, -0.5 op_sel_hi:[1,0]
	v_pk_add_f16 v181, v181, -0.5 op_sel_hi:[1,0]
	v_pk_mul_f16 v197, v181, v181
	v_pk_mul_f16 v213, v165, v181
	v_pk_fma_f16 v197, v165, v165, v197
	v_cvt_pk_f16_f32 v169, v45, v49
	v_cvt_pk_f16_f32 v185, v77, v81
	v_pk_add_f16 v169, v169, -0.5 op_sel_hi:[1,0]
	v_pk_add_f16 v185, v185, -0.5 op_sel_hi:[1,0]
	v_pk_mul_f16 v201, v185, v185
	v_pk_mul_f16 v217, v169, v185
	v_pk_fma_f16 v201, v169, v169, v201
	v_cvt_pk_f16_f32 v173, v46, v50
	v_cvt_pk_f16_f32 v189, v78, v82
	v_pk_add_f16 v173, v173, -0.5 op_sel_hi:[1,0]
	v_pk_add_f16 v189, v189, -0.5 op_sel_hi:[1,0]
	v_pk_mul_f16 v205, v189, v189
	v_pk_mul_f16 v221, v173, v189
	v_pk_fma_f16 v205, v173, v173, v205
	v_cvt_pk_f16_f32 v177, v47, v51
	v_cvt_pk_f16_f32 v193, v79, v83
	v_pk_add_f16 v177, v177, -0.5 op_sel_hi:[1,0]
	v_pk_add_f16 v193, v193, -0.5 op_sel_hi:[1,0]
	v_pk_mul_f16 v209, v193, v193
	v_pk_mul_f16 v225, v177, v193
	v_pk_fma_f16 v209, v177, v177, v209
	s_waitcnt vmcnt(16)
	v_cvt_pk_f16_f32 v166, v52, v56
	v_cvt_pk_f16_f32 v182, v84, v88
	v_pk_add_f16 v166, v166, -0.5 op_sel_hi:[1,0]
	v_pk_add_f16 v182, v182, -0.5 op_sel_hi:[1,0]
	v_pk_mul_f16 v198, v182, v182
	v_pk_mul_f16 v214, v166, v182
	v_pk_fma_f16 v198, v166, v166, v198
	v_cvt_pk_f16_f32 v170, v53, v57
	v_cvt_pk_f16_f32 v186, v85, v89
	v_pk_add_f16 v170, v170, -0.5 op_sel_hi:[1,0]
	v_pk_add_f16 v186, v186, -0.5 op_sel_hi:[1,0]
	v_pk_mul_f16 v202, v186, v186
	v_pk_mul_f16 v218, v170, v186
	v_pk_fma_f16 v202, v170, v170, v202
	v_cvt_pk_f16_f32 v174, v54, v58
	v_cvt_pk_f16_f32 v190, v86, v90
	v_pk_add_f16 v174, v174, -0.5 op_sel_hi:[1,0]
	v_pk_add_f16 v190, v190, -0.5 op_sel_hi:[1,0]
	v_pk_mul_f16 v206, v190, v190
	v_pk_mul_f16 v222, v174, v190
	v_pk_fma_f16 v206, v174, v174, v206
	v_cvt_pk_f16_f32 v178, v55, v59
	v_cvt_pk_f16_f32 v194, v87, v91
	v_pk_add_f16 v178, v178, -0.5 op_sel_hi:[1,0]
	v_pk_add_f16 v194, v194, -0.5 op_sel_hi:[1,0]
	v_pk_mul_f16 v210, v194, v194
	v_pk_mul_f16 v226, v178, v194
	v_pk_fma_f16 v210, v178, v178, v210
	s_waitcnt vmcnt(16)
	v_cvt_pk_f16_f32 v167, v60, v64
	v_cvt_pk_f16_f32 v183, v92, v96
	v_pk_add_f16 v167, v167, -0.5 op_sel_hi:[1,0]
	v_pk_add_f16 v183, v183, -0.5 op_sel_hi:[1,0]
	v_pk_mul_f16 v199, v183, v183
	v_pk_mul_f16 v215, v167, v183
	v_pk_fma_f16 v199, v167, v167, v199
	v_cvt_pk_f16_f32 v171, v61, v65
	v_cvt_pk_f16_f32 v187, v93, v97
	v_pk_add_f16 v171, v171, -0.5 op_sel_hi:[1,0]
	v_pk_add_f16 v187, v187, -0.5 op_sel_hi:[1,0]
	v_pk_mul_f16 v203, v187, v187
	v_pk_mul_f16 v219, v171, v187
	v_pk_fma_f16 v203, v171, v171, v203
	v_cvt_pk_f16_f32 v175, v62, v66
	v_cvt_pk_f16_f32 v191, v94, v98
	v_pk_add_f16 v175, v175, -0.5 op_sel_hi:[1,0]
	v_pk_add_f16 v191, v191, -0.5 op_sel_hi:[1,0]
	v_pk_mul_f16 v207, v191, v191
	v_pk_mul_f16 v223, v175, v191
	v_pk_fma_f16 v207, v175, v175, v207
	v_cvt_pk_f16_f32 v179, v63, v67
	v_cvt_pk_f16_f32 v195, v95, v99
	v_pk_add_f16 v179, v179, -0.5 op_sel_hi:[1,0]
	v_pk_add_f16 v195, v195, -0.5 op_sel_hi:[1,0]
	v_pk_mul_f16 v211, v195, v195
	v_pk_mul_f16 v227, v179, v195
	v_pk_fma_f16 v211, v179, v179, v211
	v_mfma_f32_16x16x32_f16 v[68:71], v[164:167], v[24:27], 0
	v_mfma_f32_16x16x32_f16 v[72:75], v[168:171], v[24:27], 0
	v_mfma_f32_16x16x32_f16 v[76:79], v[172:175], v[24:27], 0
	v_mfma_f32_16x16x32_f16 v[80:83], v[176:179], v[24:27], 0
	v_mfma_f32_16x16x32_f16 v[84:87], v[180:183], v[24:27], 0
	v_mfma_f32_16x16x32_f16 v[88:91], v[184:187], v[24:27], 0
	v_mfma_f32_16x16x32_f16 v[92:95], v[188:191], v[24:27], 0
	v_mfma_f32_16x16x32_f16 v[96:99], v[192:195], v[24:27], 0
	s_nop 1
	v_cvt_pk_f16_f32 v36, v68, v72
	s_nop 0
	v_cvt_pk_f16_f32 v37, v76, v80
	v_cvt_pk_f16_f32 v38, v69, v73
	v_cvt_pk_f16_f32 v39, v77, v81
	v_cvt_pk_f16_f32 v40, v70, v74
	v_cvt_pk_f16_f32 v41, v78, v82
	v_cvt_pk_f16_f32 v42, v71, v75
	v_cvt_pk_f16_f32 v43, v79, v83
	v_mfma_f32_16x16x32_f16 v[68:71], v[196:199], v[24:27], 0
	v_mfma_f32_16x16x32_f16 v[72:75], v[200:203], v[24:27], 0
	v_mfma_f32_16x16x32_f16 v[76:79], v[204:207], v[24:27], 0
	v_mfma_f32_16x16x32_f16 v[80:83], v[208:211], v[24:27], 0
	v_cvt_pk_f16_f32 v44, v84, v88
	v_cvt_pk_f16_f32 v45, v92, v96
	v_cvt_pk_f16_f32 v46, v85, v89
	v_cvt_pk_f16_f32 v47, v93, v97
	v_cvt_pk_f16_f32 v48, v86, v90
	v_cvt_pk_f16_f32 v49, v94, v98
	v_cvt_pk_f16_f32 v50, v87, v91
	v_cvt_pk_f16_f32 v51, v95, v99
	v_mfma_f32_16x16x32_f16 v[84:87], v[212:215], v[24:27], 0
	v_mfma_f32_16x16x32_f16 v[88:91], v[216:219], v[24:27], 0
	v_mfma_f32_16x16x32_f16 v[92:95], v[220:223], v[24:27], 0
	v_mfma_f32_16x16x32_f16 v[96:99], v[224:227], v[24:27], 0
	v_cvt_pk_f16_f32 v52, v68, v72
	v_cvt_pk_f16_f32 v53, v76, v80
	v_cvt_pk_f16_f32 v54, v69, v73
	v_cvt_pk_f16_f32 v55, v77, v81
	v_cvt_pk_f16_f32 v56, v70, v74
	v_cvt_pk_f16_f32 v57, v78, v82
	v_cvt_pk_f16_f32 v58, v71, v75
	v_cvt_pk_f16_f32 v59, v79, v83
	v_cvt_pk_f16_f32 v60, v84, v88
	v_cvt_pk_f16_f32 v61, v92, v96
	v_cvt_pk_f16_f32 v62, v85, v89
	v_cvt_pk_f16_f32 v63, v93, v97
	v_cvt_pk_f16_f32 v64, v86, v90
	v_cvt_pk_f16_f32 v65, v94, v98
	v_cvt_pk_f16_f32 v66, v87, v91
	v_cvt_pk_f16_f32 v67, v95, v99
	s_mov_b64 exec, s[38:39]
	ds_write_b128 v4, v[40:43] offset:0
	ds_write_b128 v4, v[48:51] offset:512
	ds_write_b128 v4, v[56:59] offset:1024
	ds_write_b128 v4, v[64:67] offset:1536
	s_mov_b64 exec, -1
	v_mfma_f32_16x16x32_f16 v[68:71], v[24:27], v[36:39], 0
	v_mfma_f32_16x16x32_f16 v[72:75], v[24:27], v[44:47], 0
	v_mfma_f32_16x16x32_f16 v[76:79], v[24:27], v[52:55], v[0:3]
	v_mfma_f32_16x16x32_f16 v[80:83], v[24:27], v[60:63], 0
	v_mfma_f32_16x16x32_f16 v[84:87], v[28:31], v[36:39], 0
	v_mfma_f32_16x16x32_f16 v[88:91], v[28:31], v[44:47], 0
	v_mfma_f32_16x16x32_f16 v[92:95], v[28:31], v[52:55], v[0:3]
	v_mfma_f32_16x16x32_f16 v[96:99], v[28:31], v[60:63], 0
	v_mfma_f32_16x16x32_f16 v[84:87], v[32:35], v[40:43], v[84:87]
	v_mfma_f32_16x16x32_f16 v[88:91], v[32:35], v[48:51], v[88:91]
	v_mfma_f32_16x16x32_f16 v[92:95], v[32:35], v[56:59], v[92:95]
	v_mfma_f32_16x16x32_f16 v[96:99], v[32:35], v[64:67], v[96:99]
	s_waitcnt lgkmcnt(0)
	ds_write_b32 v6, v6 offset:0
	ds_read_b32 v9, v7 offset:0
	v_mul_f32_e32 v244, v68, v72
	v_mul_f32_e32 v250, v69, v73
	v_mul_f32_e64 v245, -v72, v72
	v_mul_f32_e64 v251, -v73, v73
	v_add_f32_e32 v246, v68, v72
	v_add_f32_e32 v252, v69, v73
	v_fma_f32 v245, -v68, v68, v245
	v_fma_f32 v251, -v69, v69, v251
	v_fma_f32 v247, v10, v246, v11
	v_fma_f32 v253, v10, v252, v11
	v_fma_f32 v246, v13, v80, v14
	v_fma_f32 v252, v13, v81, v14
	v_fma_f32 v248, v12, v76, v245
	v_fma_f32 v254, v12, v77, v251
	v_fma_f32 v249, 2.0, v244, v247
	v_fma_f32 v255, 2.0, v250, v253
	v_sub_f32_e32 v247, v247, v245
	v_sub_f32_e32 v253, v253, v251
	v_fma_f32 v246, -2.0, v244, v246
	v_fma_f32 v252, -2.0, v250, v252
	v_mul_f32_e32 v247, v247, v248
	v_mul_f32_e32 v253, v253, v254
	v_rcp_f32_e32 v247, v247
	v_rcp_f32_e32 v253, v253
	v_mul_f32_e32 v249, v249, v246
	v_mul_f32_e32 v255, v255, v252
	v_fma_f32 v19, v249, v247, v19
	v_fma_f32 v19, v255, v253, v19
	v_mul_f32_e32 v244, v70, v74
	v_mul_f32_e32 v250, v71, v75
	v_mul_f32_e64 v245, -v74, v74
	v_mul_f32_e64 v251, -v75, v75
	v_add_f32_e32 v246, v70, v74
	v_add_f32_e32 v252, v71, v75
	v_fma_f32 v245, -v70, v70, v245
	v_fma_f32 v251, -v71, v71, v251
	v_fma_f32 v247, v10, v246, v11
	v_fma_f32 v253, v10, v252, v11
	v_fma_f32 v246, v13, v82, v14
	v_fma_f32 v252, v13, v83, v14
	v_fma_f32 v248, v12, v78, v245
	v_fma_f32 v254, v12, v79, v251
	v_fma_f32 v249, 2.0, v244, v247
	v_fma_f32 v255, 2.0, v250, v253
	v_sub_f32_e32 v247, v247, v245
	v_sub_f32_e32 v253, v253, v251
	v_fma_f32 v246, -2.0, v244, v246
	v_fma_f32 v252, -2.0, v250, v252
	v_mul_f32_e32 v247, v247, v248
	v_mul_f32_e32 v253, v253, v254
	v_rcp_f32_e32 v247, v247
	v_rcp_f32_e32 v253, v253
	v_mul_f32_e32 v249, v249, v246
	v_mul_f32_e32 v255, v255, v252
	v_fma_f32 v20, v249, v247, v20
	v_fma_f32 v20, v255, v253, v20
	v_mfma_f32_16x16x32_f16 v[68:71], v[24:27], v[40:43], 0
	v_mfma_f32_16x16x32_f16 v[72:75], v[24:27], v[48:51], 0
	v_mfma_f32_16x16x32_f16 v[76:79], v[24:27], v[56:59], v[0:3]
	v_mfma_f32_16x16x32_f16 v[80:83], v[24:27], v[64:67], 0
	s_barrier
	ds_read_b32 v9, v7 offset:0
	s_waitcnt lgkmcnt(0)
	v_cmp_ne_u32_e32 vcc, 0, v9
	s_cbranch_vccnz .Lq_go_0
